# indexer radix select: shorter histogram-accumulate per key (shift/sub/min), placement pads keep later code at the same byte phase
# speedup vs baseline: 1.0061x; 1.0012x over previous
.LBB0_1044:
	v_lshrrev_b32_e32 v5, s33, v174
	v_sub_u32_e32 v5, v5, v0
	v_min_u32_e32 v5, v5, v26
	v_lshl_add_u32 v5, v5, 2, v27
	ds_add_u32 v5, v232
	v_lshrrev_b32_e32 v5, s33, v173
	v_sub_u32_e32 v5, v5, v0
	v_min_u32_e32 v5, v5, v26
	v_lshl_add_u32 v5, v5, 2, v27
	ds_add_u32 v5, v232
	v_lshrrev_b32_e32 v5, s33, v176
	v_sub_u32_e32 v5, v5, v0
	v_min_u32_e32 v5, v5, v26
	v_lshl_add_u32 v5, v5, 2, v27
	ds_add_u32 v5, v232
	v_lshrrev_b32_e32 v5, s33, v175
	v_sub_u32_e32 v5, v5, v0
	v_min_u32_e32 v5, v5, v26
	v_lshl_add_u32 v5, v5, 2, v27
	ds_add_u32 v5, v232
	v_lshrrev_b32_e32 v5, s33, v178
	v_sub_u32_e32 v5, v5, v0
	v_min_u32_e32 v5, v5, v26
	v_lshl_add_u32 v5, v5, 2, v27
	ds_add_u32 v5, v232
	v_lshrrev_b32_e32 v5, s33, v177
	v_sub_u32_e32 v5, v5, v0
	v_min_u32_e32 v5, v5, v26
	v_lshl_add_u32 v5, v5, 2, v27
	ds_add_u32 v5, v232
	v_lshrrev_b32_e32 v5, s33, v180
	v_sub_u32_e32 v5, v5, v0
	v_min_u32_e32 v5, v5, v26
	v_lshl_add_u32 v5, v5, 2, v27
	ds_add_u32 v5, v232
	v_lshrrev_b32_e32 v5, s33, v179
	v_sub_u32_e32 v5, v5, v0
	v_min_u32_e32 v5, v5, v26
	v_lshl_add_u32 v5, v5, 2, v27
	ds_add_u32 v5, v232
	v_lshrrev_b32_e32 v5, s33, v182
	v_sub_u32_e32 v5, v5, v0
	v_min_u32_e32 v5, v5, v26
	v_lshl_add_u32 v5, v5, 2, v27
	ds_add_u32 v5, v232
	v_lshrrev_b32_e32 v5, s33, v181
	v_sub_u32_e32 v5, v5, v0
	v_min_u32_e32 v5, v5, v26
	v_lshl_add_u32 v5, v5, 2, v27
	ds_add_u32 v5, v232
	v_lshrrev_b32_e32 v5, s33, v184
	v_sub_u32_e32 v5, v5, v0
	v_min_u32_e32 v5, v5, v26
	v_lshl_add_u32 v5, v5, 2, v27
	ds_add_u32 v5, v232
	v_lshrrev_b32_e32 v5, s33, v183
	v_sub_u32_e32 v5, v5, v0
	v_min_u32_e32 v5, v5, v26
	v_lshl_add_u32 v5, v5, 2, v27
	ds_add_u32 v5, v232
	v_lshrrev_b32_e32 v5, s33, v186
	v_sub_u32_e32 v5, v5, v0
	v_min_u32_e32 v5, v5, v26
	v_lshl_add_u32 v5, v5, 2, v27
	ds_add_u32 v5, v232
	v_lshrrev_b32_e32 v5, s33, v185
	v_sub_u32_e32 v5, v5, v0
	v_min_u32_e32 v5, v5, v26
	v_lshl_add_u32 v5, v5, 2, v27
	ds_add_u32 v5, v232
	v_lshrrev_b32_e32 v5, s33, v188
	v_sub_u32_e32 v5, v5, v0
	v_min_u32_e32 v5, v5, v26
	v_lshl_add_u32 v5, v5, 2, v27
	ds_add_u32 v5, v232
	v_lshrrev_b32_e32 v5, s33, v187
	v_sub_u32_e32 v5, v5, v0
	v_min_u32_e32 v5, v5, v26
	v_lshl_add_u32 v5, v5, 2, v27
	ds_add_u32 v5, v232
	s_nop 0
	s_andn2_b64 vcc, exec, s[62:63]
	s_cbranch_vccz .LBB0_980
	s_branch .LBB0_981
